# P10 combine loop: routing records fetched one token ahead; expert-row gathers issued at the loop top beside the x2 loads (one round trip per token)
# baseline (speedup 1.0000x reference)
.LBB0_1478:
	s_or_b64 exec, exec, s[0:1]
	s_andn2_b64 vcc, exec, s[92:93]
	s_waitcnt lgkmcnt(0)
	s_barrier
	s_cbranch_vccnz .LBB0_1481
	v_and_b32_e32 v1, 63, v0
	v_lshlrev_b32_e32 v2, 2, v0
	v_lshlrev_b32_e32 v16, 3, v1
	v_lshrrev_b32_e32 v0, 2, v0
	v_and_b32_e32 v2, 4, v2
	v_and_b32_e32 v3, 0xf0, v16
	v_and_b32_e32 v0, 8, v0
	v_or3_b32 v4, v3, v0, v2
	v_mbcnt_hi_u32_b32 v0, -1, v228
	v_and_b32_e32 v2, 64, v0
	v_add_u32_e32 v2, 64, v2
	v_xor_b32_e32 v3, 32, v0
	v_cmp_lt_i32_e32 vcc, v3, v2
	s_ashr_i32 s91, s90, 31
	s_ashr_i32 s89, s88, 31
	v_cndmask_b32_e32 v3, v0, v3, vcc
	v_lshlrev_b32_e32 v22, 2, v3
	v_xor_b32_e32 v3, 16, v0
	v_cmp_lt_i32_e32 vcc, v3, v2
	s_lshl_b64 s[6:7], s[90:91], 12
	s_lshl_b64 s[0:1], s[90:91], 6
	v_cndmask_b32_e32 v3, v0, v3, vcc
	v_lshlrev_b32_e32 v23, 2, v3
	v_xor_b32_e32 v3, 8, v0
	v_cmp_lt_i32_e32 vcc, v3, v2
	s_lshl_b64 s[2:3], s[88:89], 6
	v_or_b32_e32 v16, s6, v16
	v_cndmask_b32_e32 v3, v0, v3, vcc
	v_lshlrev_b32_e32 v24, 2, v3
	v_xor_b32_e32 v3, 4, v0
	v_cmp_lt_i32_e32 vcc, v3, v2
	v_mov_b32_e32 v17, s7
	s_lshl_b64 s[6:7], s[88:89], 12
	v_cndmask_b32_e32 v3, v0, v3, vcc
	v_lshlrev_b32_e32 v25, 2, v3
	v_xor_b32_e32 v3, 2, v0
	v_cmp_lt_i32_e32 vcc, v3, v2
	s_lshl_b64 s[8:9], s[90:91], 13
	s_add_u32 s8, s82, s8
	v_cndmask_b32_e32 v3, v0, v3, vcc
	v_lshlrev_b32_e32 v26, 2, v3
	v_xor_b32_e32 v3, 1, v0
	v_cmp_lt_i32_e32 vcc, v3, v2
	s_addc_u32 s9, s83, s9
	v_mov_b32_e32 v28, 0x45200000
	v_cndmask_b32_e32 v0, v0, v3, vcc
	v_lshlrev_b32_e32 v27, 2, v0
	v_lshlrev_b32_e32 v0, 4, v1
	v_mov_b32_e32 v1, 0
	v_or_b32_e32 v2, 0x1000, v0
	v_mov_b32_e32 v3, v1
	v_lshl_add_u64 v[8:9], s[80:81], 0, v[2:3]
	v_or_b32_e32 v2, 0x1400, v0
	v_lshl_add_u64 v[10:11], s[80:81], 0, v[2:3]
	v_or_b32_e32 v2, 0x1800, v0
	v_lshl_add_u64 v[6:7], s[80:81], 0, v[0:1]
	v_mov_b32_e32 v5, v1
	v_lshl_add_u64 v[12:13], s[80:81], 0, v[2:3]
	v_or_b32_e32 v2, 0x1c00, v0
	v_lshl_add_u64 v[0:1], s[8:9], 0, v[0:1]
	s_mov_b64 s[8:9], 0x1000
	v_lshl_add_u64 v[14:15], s[80:81], 0, v[2:3]
	v_lshl_add_u64 v[18:19], v[0:1], 0, s[8:9]
	s_lshl_b64 s[8:9], s[88:89], 13
	s_add_i32 s12, 0, 0x20080
	v_mov_b32_e32 v29, 0x3727c5ac
	global_load_dwordx4 v[196:199], v[6:7], off
	global_load_dwordx4 v[200:203], v[6:7], off offset:1024
	global_load_dwordx4 v[204:207], v[6:7], off offset:2048
	global_load_dwordx4 v[208:211], v[6:7], off offset:3072
	global_load_dwordx4 v[212:215], v[8:9], off
	global_load_dwordx4 v[216:219], v[10:11], off
	global_load_dwordx4 v[220:223], v[12:13], off
	global_load_dwordx4 v[224:227], v[14:15], off
	s_add_u32 s10, s84, s0
	s_addc_u32 s11, s85, s1
	global_load_dwordx3 v[230:232], v28, s[10:11]
	global_load_dwordx3 v[234:236], v28, s[10:11] offset:16
	global_load_dwordx3 v[238:240], v28, s[10:11] offset:32
	global_load_dwordx3 v[242:244], v28, s[10:11] offset:48
.LBB0_1480:
	v_lshl_add_u64 v[20:21], s[84:85], 0, v[16:17]
	v_add_co_u32_e32 v20, vcc, 0x2d400000, v20
	s_add_i32 s90, s90, s88
	s_add_u32 s0, s0, s2
	s_addc_u32 s1, s1, s3
	v_addc_co_u32_e32 v21, vcc, 0, v21, vcc
	global_load_dwordx2 v[46:47], v[20:21], off nt
	global_load_dwordx2 v[48:49], v[20:21], off offset:512 nt
	global_load_dwordx2 v[50:51], v[20:21], off offset:1024 nt
	global_load_dwordx2 v[52:53], v[20:21], off offset:1536 nt
	global_load_dwordx2 v[54:55], v[20:21], off offset:2048 nt
	global_load_dwordx2 v[56:57], v[20:21], off offset:2560 nt
	global_load_dwordx2 v[58:59], v[20:21], off offset:3584 nt
	global_load_dwordx2 v[60:61], v[20:21], off offset:3072 nt
	s_add_u32 s10, s84, s0
	s_addc_u32 s11, s85, s1
	v_lshl_add_u64 v[16:17], v[16:17], 0, s[6:7]
	s_cmpk_lt_i32 s90, 0x4000
	s_waitcnt vmcnt(8)
	v_mov_b32_e32 v30, v230
	v_mov_b32_e32 v31, v231
	v_mov_b32_e32 v32, v232
	v_mov_b32_e32 v34, v234
	v_mov_b32_e32 v35, v235
	v_mov_b32_e32 v36, v236
	v_mov_b32_e32 v38, v238
	v_mov_b32_e32 v39, v239
	v_mov_b32_e32 v40, v240
	v_mov_b32_e32 v42, v242
	v_mov_b32_e32 v43, v243
	v_mov_b32_e32 v44, v244
	global_load_dwordx3 v[230:232], v28, s[10:11]
	global_load_dwordx3 v[234:236], v28, s[10:11] offset:16
	global_load_dwordx3 v[238:240], v28, s[10:11] offset:32
	global_load_dwordx3 v[242:244], v28, s[10:11] offset:48
	v_lshlrev_b32_e32 v21, 2, v30
	v_lshlrev_b32_e32 v33, 2, v34
	v_lshlrev_b32_e32 v37, 2, v38
	v_lshlrev_b32_e32 v41, 2, v42
	v_add_u32_e32 v21, s12, v21
	v_add_u32_e32 v33, s12, v33
	v_add_u32_e32 v37, s12, v37
	v_add_u32_e32 v41, s12, v41
	ds_read_b32 v246, v21
	ds_read_b32 v78, v33
	ds_read_b32 v80, v37
	ds_read_b32 v82, v41
	s_waitcnt lgkmcnt(3)
	v_ashrrev_i32_e32 v247, 31, v246
	v_ashrrev_i32_e32 v63, 31, v31
	v_mov_b32_e32 v62, v31
	s_waitcnt lgkmcnt(2)
	v_ashrrev_i32_e32 v79, 31, v78
	s_waitcnt lgkmcnt(1)
	v_ashrrev_i32_e32 v81, 31, v80
	s_waitcnt lgkmcnt(0)
	v_ashrrev_i32_e32 v83, 31, v82
	v_lshlrev_b64 v[246:247], 19, v[246:247]
	v_ashrrev_i32_e32 v31, 31, v35
	v_mov_b32_e32 v30, v35
	v_ashrrev_i32_e32 v35, 31, v39
	v_mov_b32_e32 v34, v39
	v_ashrrev_i32_e32 v39, 31, v43
	v_mov_b32_e32 v38, v43
	v_lshlrev_b64 v[42:43], 11, v[62:63]
	v_lshlrev_b64 v[78:79], 19, v[78:79]
	v_lshlrev_b64 v[80:81], 19, v[80:81]
	v_lshlrev_b64 v[82:83], 19, v[82:83]
	v_lshl_add_u64 v[246:247], s[4:5], 0, v[246:247]
	v_lshlrev_b64 v[30:31], 11, v[30:31]
	v_lshlrev_b64 v[34:35], 11, v[34:35]
	v_lshlrev_b64 v[38:39], 11, v[38:39]
	v_lshl_add_u64 v[78:79], s[4:5], 0, v[78:79]
	v_lshl_add_u64 v[80:81], s[4:5], 0, v[80:81]
	v_lshl_add_u64 v[82:83], s[4:5], 0, v[82:83]
	v_lshl_add_u64 v[42:43], v[246:247], 0, v[42:43]
	v_lshl_add_u64 v[30:31], v[78:79], 0, v[30:31]
	v_lshl_add_u64 v[34:35], v[80:81], 0, v[34:35]
	v_lshl_add_u64 v[38:39], v[82:83], 0, v[38:39]
	v_lshl_add_u64 v[42:43], v[42:43], 0, v[4:5]
	v_lshl_add_u64 v[30:31], v[30:31], 0, v[4:5]
	v_lshl_add_u64 v[34:35], v[34:35], 0, v[4:5]
	v_lshl_add_u64 v[38:39], v[38:39], 0, v[4:5]
	global_load_dword v21, v[42:43], off nt
	global_load_dword v33, v[42:43], off offset:256 nt
	global_load_dword v37, v[42:43], off offset:512 nt
	global_load_dword v41, v[42:43], off offset:768 nt
	global_load_dword v86, v[42:43], off offset:1024 nt
	global_load_dword v90, v[42:43], off offset:1280 nt
	global_load_dword v94, v[42:43], off offset:1536 nt
	global_load_dword v98, v[42:43], off offset:1792 nt
	global_load_dword v102, v[30:31], off nt
	global_load_dword v106, v[30:31], off offset:256 nt
	global_load_dword v110, v[30:31], off offset:512 nt
	global_load_dword v114, v[30:31], off offset:768 nt
	global_load_dword v118, v[30:31], off offset:1024 nt
	global_load_dword v122, v[30:31], off offset:1280 nt
	global_load_dword v126, v[30:31], off offset:1536 nt
	global_load_dword v130, v[30:31], off offset:1792 nt
	global_load_dword v134, v[34:35], off nt
	global_load_dword v138, v[34:35], off offset:256 nt
	global_load_dword v142, v[34:35], off offset:512 nt
	global_load_dword v146, v[34:35], off offset:768 nt
	global_load_dword v150, v[34:35], off offset:1024 nt
	global_load_dword v154, v[34:35], off offset:1280 nt
	global_load_dword v158, v[34:35], off offset:1536 nt
	global_load_dword v162, v[34:35], off offset:1792 nt
	global_load_dword v166, v[38:39], off nt
	global_load_dword v170, v[38:39], off offset:256 nt
	global_load_dword v174, v[38:39], off offset:512 nt
	global_load_dword v178, v[38:39], off offset:768 nt
	global_load_dword v182, v[38:39], off offset:1024 nt
	global_load_dword v186, v[38:39], off offset:1280 nt
	global_load_dword v190, v[38:39], off offset:1536 nt
	global_load_dword v194, v[38:39], off offset:1792 nt
	s_waitcnt vmcnt(36)
	v_and_b32_e32 v45, 0xffff0000, v46
	v_lshlrev_b32_e32 v72, 16, v60
	v_and_b32_e32 v74, 0xffff0000, v60
	v_lshlrev_b32_e32 v73, 16, v58
	v_and_b32_e32 v75, 0xffff0000, v58
	v_lshlrev_b32_e32 v76, 16, v61
	v_and_b32_e32 v58, 0xffff0000, v61
	v_mov_b32_e32 v20, v44
	v_lshlrev_b32_e32 v44, 16, v46
	v_lshlrev_b32_e32 v62, 16, v48
	v_and_b32_e32 v63, 0xffff0000, v48
	v_lshlrev_b32_e32 v46, 16, v47
	v_and_b32_e32 v47, 0xffff0000, v47
	v_lshlrev_b32_e32 v48, 16, v49
	v_and_b32_e32 v49, 0xffff0000, v49
	v_lshlrev_b32_e32 v64, 16, v50
	v_and_b32_e32 v65, 0xffff0000, v50
	v_lshlrev_b32_e32 v50, 16, v51
	v_and_b32_e32 v51, 0xffff0000, v51
	v_lshlrev_b32_e32 v66, 16, v52
	v_and_b32_e32 v67, 0xffff0000, v52
	v_lshlrev_b32_e32 v52, 16, v53
	v_and_b32_e32 v53, 0xffff0000, v53
	v_lshlrev_b32_e32 v68, 16, v54
	v_and_b32_e32 v69, 0xffff0000, v54
	v_lshlrev_b32_e32 v54, 16, v55
	v_and_b32_e32 v55, 0xffff0000, v55
	v_lshlrev_b32_e32 v70, 16, v56
	v_and_b32_e32 v71, 0xffff0000, v56
	v_lshlrev_b32_e32 v56, 16, v57
	v_and_b32_e32 v57, 0xffff0000, v57
	v_lshlrev_b32_e32 v77, 16, v59
	v_and_b32_e32 v59, 0xffff0000, v59
	s_waitcnt vmcnt(31)
	v_cvt_pk_f32_fp8_e32 v[30:31], v21
	s_waitcnt vmcnt(30)
	v_cvt_pk_f32_fp8_e32 v[38:39], v33
	v_cvt_pk_f32_fp8_sdwa v[34:35], v21 src0_sel:WORD_1
	v_cvt_pk_f32_fp8_sdwa v[42:43], v33 src0_sel:WORD_1
	s_waitcnt vmcnt(29)
	v_cvt_pk_f32_fp8_e32 v[60:61], v37
	v_cvt_pk_f32_fp8_sdwa v[78:79], v37 src0_sel:WORD_1
	s_waitcnt vmcnt(28)
	v_cvt_pk_f32_fp8_e32 v[80:81], v41
	v_cvt_pk_f32_fp8_sdwa v[82:83], v41 src0_sel:WORD_1
	s_waitcnt vmcnt(27)
	v_cvt_pk_f32_fp8_e32 v[84:85], v86
	v_cvt_pk_f32_fp8_sdwa v[86:87], v86 src0_sel:WORD_1
	s_waitcnt vmcnt(26)
	v_cvt_pk_f32_fp8_e32 v[88:89], v90
	s_waitcnt vmcnt(25)
	v_cvt_pk_f32_fp8_e32 v[92:93], v94
	v_cvt_pk_f32_fp8_sdwa v[94:95], v94 src0_sel:WORD_1
	s_waitcnt vmcnt(24)
	v_cvt_pk_f32_fp8_e32 v[96:97], v98
	v_cvt_pk_f32_fp8_sdwa v[98:99], v98 src0_sel:WORD_1
	s_waitcnt vmcnt(23)
	v_cvt_pk_f32_fp8_e32 v[100:101], v102
	s_waitcnt vmcnt(22)
	v_cvt_pk_f32_fp8_e32 v[104:105], v106
	v_cvt_pk_f32_fp8_sdwa v[90:91], v90 src0_sel:WORD_1
	v_cvt_pk_f32_fp8_sdwa v[102:103], v102 src0_sel:WORD_1
	v_cvt_pk_f32_fp8_sdwa v[106:107], v106 src0_sel:WORD_1
	s_waitcnt vmcnt(21)
	v_cvt_pk_f32_fp8_e32 v[108:109], v110
	v_cvt_pk_f32_fp8_sdwa v[110:111], v110 src0_sel:WORD_1
	s_waitcnt vmcnt(20)
	v_cvt_pk_f32_fp8_e32 v[112:113], v114
	v_cvt_pk_f32_fp8_sdwa v[114:115], v114 src0_sel:WORD_1
	s_waitcnt vmcnt(19)
	v_cvt_pk_f32_fp8_e32 v[116:117], v118
	v_cvt_pk_f32_fp8_sdwa v[118:119], v118 src0_sel:WORD_1
	s_waitcnt vmcnt(18)
	v_cvt_pk_f32_fp8_e32 v[120:121], v122
	s_waitcnt vmcnt(17)
	v_cvt_pk_f32_fp8_e32 v[124:125], v126
	v_cvt_pk_f32_fp8_sdwa v[126:127], v126 src0_sel:WORD_1
	s_waitcnt vmcnt(16)
	v_cvt_pk_f32_fp8_e32 v[128:129], v130
	v_cvt_pk_f32_fp8_sdwa v[130:131], v130 src0_sel:WORD_1
	s_waitcnt vmcnt(15)
	v_cvt_pk_f32_fp8_e32 v[132:133], v134
	s_waitcnt vmcnt(14)
	v_cvt_pk_f32_fp8_e32 v[136:137], v138
	v_cvt_pk_f32_fp8_sdwa v[122:123], v122 src0_sel:WORD_1
	v_cvt_pk_f32_fp8_sdwa v[134:135], v134 src0_sel:WORD_1
	v_cvt_pk_f32_fp8_sdwa v[138:139], v138 src0_sel:WORD_1
	s_waitcnt vmcnt(13)
	v_cvt_pk_f32_fp8_e32 v[140:141], v142
	v_cvt_pk_f32_fp8_sdwa v[142:143], v142 src0_sel:WORD_1
	s_waitcnt vmcnt(12)
	v_cvt_pk_f32_fp8_e32 v[144:145], v146
	v_cvt_pk_f32_fp8_sdwa v[146:147], v146 src0_sel:WORD_1
	s_waitcnt vmcnt(11)
	v_cvt_pk_f32_fp8_e32 v[148:149], v150
	v_cvt_pk_f32_fp8_sdwa v[150:151], v150 src0_sel:WORD_1
	s_waitcnt vmcnt(10)
	v_cvt_pk_f32_fp8_e32 v[152:153], v154
	s_waitcnt vmcnt(9)
	v_cvt_pk_f32_fp8_e32 v[156:157], v158
	v_cvt_pk_f32_fp8_sdwa v[158:159], v158 src0_sel:WORD_1
	s_waitcnt vmcnt(8)
	v_cvt_pk_f32_fp8_e32 v[160:161], v162
	v_cvt_pk_f32_fp8_sdwa v[162:163], v162 src0_sel:WORD_1
	s_waitcnt vmcnt(7)
	v_cvt_pk_f32_fp8_e32 v[164:165], v166
	s_waitcnt vmcnt(6)
	v_cvt_pk_f32_fp8_e32 v[168:169], v170
	v_cvt_pk_f32_fp8_sdwa v[154:155], v154 src0_sel:WORD_1
	v_cvt_pk_f32_fp8_sdwa v[166:167], v166 src0_sel:WORD_1
	v_cvt_pk_f32_fp8_sdwa v[170:171], v170 src0_sel:WORD_1
	s_waitcnt vmcnt(5)
	v_cvt_pk_f32_fp8_e32 v[172:173], v174
	v_cvt_pk_f32_fp8_sdwa v[174:175], v174 src0_sel:WORD_1
	s_waitcnt vmcnt(4)
	v_cvt_pk_f32_fp8_e32 v[176:177], v178
	v_cvt_pk_f32_fp8_sdwa v[178:179], v178 src0_sel:WORD_1
	s_waitcnt vmcnt(3)
	v_cvt_pk_f32_fp8_e32 v[180:181], v182
	v_cvt_pk_f32_fp8_sdwa v[182:183], v182 src0_sel:WORD_1
	s_waitcnt vmcnt(2)
	v_cvt_pk_f32_fp8_e32 v[184:185], v186
	v_pk_fma_f32 v[30:31], v[32:33], v[30:31], v[44:45] op_sel_hi:[0,1,1]
	v_pk_fma_f32 v[38:39], v[32:33], v[38:39], v[62:63] op_sel_hi:[0,1,1]
	v_pk_fma_f32 v[34:35], v[32:33], v[34:35], v[46:47] op_sel_hi:[0,1,1]
	v_pk_fma_f32 v[42:43], v[32:33], v[42:43], v[48:49] op_sel_hi:[0,1,1]
	v_pk_fma_f32 v[44:45], v[32:33], v[60:61], v[64:65] op_sel_hi:[0,1,1]
	v_pk_fma_f32 v[46:47], v[32:33], v[78:79], v[50:51] op_sel_hi:[0,1,1]
	v_pk_fma_f32 v[48:49], v[32:33], v[80:81], v[66:67] op_sel_hi:[0,1,1]
	v_pk_fma_f32 v[50:51], v[32:33], v[82:83], v[52:53] op_sel_hi:[0,1,1]
	v_pk_fma_f32 v[52:53], v[32:33], v[84:85], v[68:69] op_sel_hi:[0,1,1]
	v_pk_fma_f32 v[54:55], v[32:33], v[86:87], v[54:55] op_sel_hi:[0,1,1]
	v_pk_fma_f32 v[60:61], v[32:33], v[88:89], v[70:71] op_sel_hi:[0,1,1]
	v_mov_b32_e32 v62, v92
	v_mov_b32_e32 v63, v96
	v_mov_b32_e32 v96, v93
	v_mov_b32_e32 v64, v94
	v_mov_b32_e32 v65, v98
	v_mov_b32_e32 v98, v95
	v_pk_fma_f32 v[30:31], v[36:37], v[100:101], v[30:31] op_sel_hi:[0,1,1]
	v_pk_fma_f32 v[38:39], v[36:37], v[104:105], v[38:39] op_sel_hi:[0,1,1]
	v_pk_fma_f32 v[56:57], v[32:33], v[90:91], v[56:57] op_sel_hi:[0,1,1]
	v_mov_b32_e32 v66, v124
	v_mov_b32_e32 v67, v128
	v_mov_b32_e32 v128, v125
	v_mov_b32_e32 v68, v126
	v_mov_b32_e32 v69, v130
	v_mov_b32_e32 v130, v127
	v_pk_fma_f32 v[34:35], v[36:37], v[102:103], v[34:35] op_sel_hi:[0,1,1]
	v_pk_fma_f32 v[42:43], v[36:37], v[106:107], v[42:43] op_sel_hi:[0,1,1]
	v_pk_fma_f32 v[44:45], v[36:37], v[108:109], v[44:45] op_sel_hi:[0,1,1]
	v_pk_fma_f32 v[46:47], v[36:37], v[110:111], v[46:47] op_sel_hi:[0,1,1]
	v_pk_fma_f32 v[48:49], v[36:37], v[112:113], v[48:49] op_sel_hi:[0,1,1]
	v_pk_fma_f32 v[50:51], v[36:37], v[114:115], v[50:51] op_sel_hi:[0,1,1]
	v_pk_fma_f32 v[52:53], v[36:37], v[116:117], v[52:53] op_sel_hi:[0,1,1]
	v_pk_fma_f32 v[54:55], v[36:37], v[118:119], v[54:55] op_sel_hi:[0,1,1]
	v_pk_fma_f32 v[60:61], v[36:37], v[120:121], v[60:61] op_sel_hi:[0,1,1]
	v_pk_fma_f32 v[62:63], v[32:33], v[62:63], v[72:73] op_sel_hi:[0,1,1]
	v_pk_fma_f32 v[72:73], v[32:33], v[96:97], v[74:75] op_sel_hi:[0,1,1]
	v_pk_fma_f32 v[64:65], v[32:33], v[64:65], v[76:77] op_sel_hi:[0,1,1]
	v_pk_fma_f32 v[32:33], v[32:33], v[98:99], v[58:59] op_sel_hi:[0,1,1]
	v_pk_fma_f32 v[30:31], v[40:41], v[132:133], v[30:31] op_sel_hi:[0,1,1]
	v_pk_fma_f32 v[38:39], v[40:41], v[136:137], v[38:39] op_sel_hi:[0,1,1]
	s_waitcnt vmcnt(1)
	v_cvt_pk_f32_fp8_e32 v[188:189], v190
	s_waitcnt vmcnt(0)
	v_cvt_pk_f32_fp8_e32 v[192:193], v194
	v_mov_b32_e32 v70, v156
	v_mov_b32_e32 v71, v160
	v_mov_b32_e32 v160, v157
	v_mov_b32_e32 v78, v158
	v_mov_b32_e32 v79, v162
	v_mov_b32_e32 v162, v159
	v_pk_fma_f32 v[56:57], v[36:37], v[122:123], v[56:57] op_sel_hi:[0,1,1]
	v_pk_fma_f32 v[34:35], v[40:41], v[134:135], v[34:35] op_sel_hi:[0,1,1]
	v_pk_fma_f32 v[42:43], v[40:41], v[138:139], v[42:43] op_sel_hi:[0,1,1]
	v_pk_fma_f32 v[44:45], v[40:41], v[140:141], v[44:45] op_sel_hi:[0,1,1]
	v_pk_fma_f32 v[46:47], v[40:41], v[142:143], v[46:47] op_sel_hi:[0,1,1]
	v_pk_fma_f32 v[48:49], v[40:41], v[144:145], v[48:49] op_sel_hi:[0,1,1]
	v_pk_fma_f32 v[50:51], v[40:41], v[146:147], v[50:51] op_sel_hi:[0,1,1]
	v_pk_fma_f32 v[52:53], v[40:41], v[148:149], v[52:53] op_sel_hi:[0,1,1]
	v_pk_fma_f32 v[54:55], v[40:41], v[150:151], v[54:55] op_sel_hi:[0,1,1]
	v_pk_fma_f32 v[58:59], v[40:41], v[152:153], v[60:61] op_sel_hi:[0,1,1]
	v_pk_fma_f32 v[60:61], v[36:37], v[66:67], v[62:63] op_sel_hi:[0,1,1]
	v_pk_fma_f32 v[62:63], v[36:37], v[128:129], v[72:73] op_sel_hi:[0,1,1]
	v_pk_fma_f32 v[64:65], v[36:37], v[68:69], v[64:65] op_sel_hi:[0,1,1]
	v_pk_fma_f32 v[32:33], v[36:37], v[130:131], v[32:33] op_sel_hi:[0,1,1]
	v_pk_fma_f32 v[30:31], v[20:21], v[164:165], v[30:31] op_sel_hi:[0,1,1]
	v_pk_fma_f32 v[36:37], v[20:21], v[168:169], v[38:39] op_sel_hi:[0,1,1]
	v_cvt_pk_f32_fp8_sdwa v[186:187], v186 src0_sel:WORD_1
	v_cvt_pk_f32_fp8_sdwa v[190:191], v190 src0_sel:WORD_1
	v_cvt_pk_f32_fp8_sdwa v[194:195], v194 src0_sel:WORD_1
	v_pk_fma_f32 v[56:57], v[40:41], v[154:155], v[56:57] op_sel_hi:[0,1,1]
	v_pk_fma_f32 v[34:35], v[20:21], v[166:167], v[34:35] op_sel_hi:[0,1,1]
	v_pk_fma_f32 v[38:39], v[20:21], v[170:171], v[42:43] op_sel_hi:[0,1,1]
	v_pk_fma_f32 v[42:43], v[20:21], v[172:173], v[44:45] op_sel_hi:[0,1,1]
	v_pk_fma_f32 v[44:45], v[20:21], v[174:175], v[46:47] op_sel_hi:[0,1,1]
	v_pk_fma_f32 v[46:47], v[20:21], v[176:177], v[48:49] op_sel_hi:[0,1,1]
	v_pk_fma_f32 v[48:49], v[20:21], v[178:179], v[50:51] op_sel_hi:[0,1,1]
	v_pk_fma_f32 v[50:51], v[20:21], v[180:181], v[52:53] op_sel_hi:[0,1,1]
	v_pk_fma_f32 v[52:53], v[20:21], v[182:183], v[54:55] op_sel_hi:[0,1,1]
	v_pk_fma_f32 v[54:55], v[20:21], v[184:185], v[58:59] op_sel_hi:[0,1,1]
	v_pk_fma_f32 v[58:59], v[40:41], v[70:71], v[60:61] op_sel_hi:[0,1,1]
	v_pk_fma_f32 v[60:61], v[40:41], v[160:161], v[62:63] op_sel_hi:[0,1,1]
	v_pk_fma_f32 v[62:63], v[40:41], v[78:79], v[64:65] op_sel_hi:[0,1,1]
	v_pk_fma_f32 v[32:33], v[40:41], v[162:163], v[32:33] op_sel_hi:[0,1,1]
	v_pk_mul_f32 v[40:41], v[30:31], v[30:31]
	v_pk_mul_f32 v[66:67], v[36:37], v[36:37]
	v_pk_mul_f32 v[64:65], v[34:35], v[34:35]
	v_pk_mul_f32 v[68:69], v[38:39], v[38:39]
	v_pk_mul_f32 v[70:71], v[42:43], v[42:43]
	v_add_f32_e32 v66, v66, v67
	v_add_f32_e32 v40, v40, v41
	v_pk_mul_f32 v[72:73], v[44:45], v[44:45]
	v_pk_mul_f32 v[74:75], v[46:47], v[46:47]
	v_add_f32_e32 v41, v70, v71
	v_add_f32_e32 v66, v68, v66
	v_add_f32_e32 v40, v64, v40
	v_mov_b32_e32 v81, v192
	v_mov_b32_e32 v192, v189
	v_pk_mul_f32 v[76:77], v[48:49], v[48:49]
	v_pk_mul_f32 v[78:79], v[50:51], v[50:51]
	v_add_f32_e32 v67, v74, v75
	v_add_f32_e32 v41, v72, v41
	v_add_f32_e32 v66, v69, v66
	v_add_f32_e32 v40, v65, v40
	v_mov_b32_e32 v80, v188
	v_mov_b32_e32 v82, v190
	v_mov_b32_e32 v83, v194
	v_mov_b32_e32 v194, v191
	v_pk_fma_f32 v[56:57], v[20:21], v[186:187], v[56:57] op_sel_hi:[0,1,1]
	v_pk_mul_f32 v[84:85], v[52:53], v[52:53]
	v_pk_mul_f32 v[86:87], v[54:55], v[54:55]
	v_pk_fma_f32 v[60:61], v[20:21], v[192:193], v[60:61] op_sel_hi:[0,1,1]
	v_add_f32_e32 v70, v78, v79
	v_add_f32_e32 v64, v76, v67
	v_add_f32_e32 v41, v73, v41
	v_add_f32_e32 v40, v40, v66
	v_pk_mul_f32 v[88:89], v[56:57], v[56:57]
	v_pk_fma_f32 v[58:59], v[20:21], v[80:81], v[58:59] op_sel_hi:[0,1,1]
	v_pk_fma_f32 v[62:63], v[20:21], v[82:83], v[62:63] op_sel_hi:[0,1,1]
	v_pk_fma_f32 v[20:21], v[20:21], v[194:195], v[32:33] op_sel_hi:[0,1,1]
	v_pk_mul_f32 v[32:33], v[60:61], v[60:61]
	v_add_f32_e32 v71, v86, v87
	v_add_f32_e32 v67, v84, v70
	v_add_f32_e32 v64, v77, v64
	v_add_f32_e32 v40, v40, v41
	v_pk_fma_f32 v[32:33], v[58:59], v[58:59], v[32:33]
	v_add_f32_e32 v68, v88, v71
	v_add_f32_e32 v65, v85, v67
	v_add_f32_e32 v40, v40, v64
	v_pk_fma_f32 v[32:33], v[62:63], v[62:63], v[32:33]
	v_add_f32_e32 v67, v89, v68
	v_add_f32_e32 v40, v40, v65
	v_pk_fma_f32 v[32:33], v[20:21], v[20:21], v[32:33]
	v_add_f32_e32 v40, v40, v67
	v_add_f32_e32 v32, v40, v32
	v_add_f32_e32 v32, v32, v33
	ds_bpermute_b32 v33, v22, v32
	s_waitcnt lgkmcnt(0)
	v_add_f32_e32 v32, v32, v33
	ds_bpermute_b32 v33, v23, v32
	s_waitcnt lgkmcnt(0)
	v_add_f32_e32 v32, v32, v33
	ds_bpermute_b32 v33, v24, v32
	s_waitcnt lgkmcnt(0)
	v_add_f32_e32 v32, v32, v33
	ds_bpermute_b32 v33, v25, v32
	s_waitcnt lgkmcnt(0)
	v_add_f32_e32 v32, v32, v33
	ds_bpermute_b32 v33, v26, v32
	s_waitcnt lgkmcnt(0)
	v_add_f32_e32 v32, v32, v33
	ds_bpermute_b32 v33, v27, v32
	s_waitcnt lgkmcnt(0)
	v_add_f32_e32 v32, v32, v33
	v_fmamk_f32 v32, v32, 0x3a000000, v29
	v_rsq_f32_e32 v32, v32
	s_nop 0
	v_pk_mul_f32 v[30:31], v[30:31], v[32:33] op_sel_hi:[1,0]
	v_pk_mul_f32 v[34:35], v[34:35], v[32:33] op_sel_hi:[1,0]
	v_pk_mul_f32 v[0:1], v[196:197], v[30:31]
	v_pk_mul_f32 v[2:3], v[198:199], v[34:35]
	global_store_dwordx4 v[18:19], v[0:3], off offset:-4096 nt
	v_pk_mul_f32 v[30:31], v[38:39], v[32:33] op_sel_hi:[1,0]
	v_pk_mul_f32 v[34:35], v[36:37], v[32:33] op_sel_hi:[1,0]
	v_pk_mul_f32 v[2:3], v[202:203], v[30:31]
	v_pk_mul_f32 v[0:1], v[200:201], v[34:35]
	global_store_dwordx4 v[18:19], v[0:3], off offset:-3072 nt
	v_pk_mul_f32 v[30:31], v[44:45], v[32:33] op_sel_hi:[1,0]
	v_pk_mul_f32 v[34:35], v[42:43], v[32:33] op_sel_hi:[1,0]
	v_pk_mul_f32 v[2:3], v[206:207], v[30:31]
	v_pk_mul_f32 v[0:1], v[204:205], v[34:35]
	global_store_dwordx4 v[18:19], v[0:3], off offset:-2048 nt
	v_pk_mul_f32 v[30:31], v[48:49], v[32:33] op_sel_hi:[1,0]
	v_pk_mul_f32 v[34:35], v[46:47], v[32:33] op_sel_hi:[1,0]
	v_pk_mul_f32 v[2:3], v[210:211], v[30:31]
	v_pk_mul_f32 v[0:1], v[208:209], v[34:35]
	global_store_dwordx4 v[18:19], v[0:3], off offset:-1024 nt
	v_pk_mul_f32 v[30:31], v[52:53], v[32:33] op_sel_hi:[1,0]
	v_pk_mul_f32 v[34:35], v[50:51], v[32:33] op_sel_hi:[1,0]
	v_pk_mul_f32 v[2:3], v[214:215], v[30:31]
	v_pk_mul_f32 v[0:1], v[212:213], v[34:35]
	global_store_dwordx4 v[18:19], v[0:3], off nt
	v_pk_mul_f32 v[30:31], v[56:57], v[32:33] op_sel_hi:[1,0]
	v_pk_mul_f32 v[34:35], v[54:55], v[32:33] op_sel_hi:[1,0]
	v_pk_mul_f32 v[2:3], v[218:219], v[30:31]
	v_pk_mul_f32 v[0:1], v[216:217], v[34:35]
	global_store_dwordx4 v[18:19], v[0:3], off offset:1024 nt
	v_mov_b32_e32 v30, v62
	v_mov_b32_e32 v31, v20
	v_mov_b32_e32 v34, v58
	v_mov_b32_e32 v35, v60
	v_pk_mul_f32 v[30:31], v[30:31], v[32:33] op_sel_hi:[1,0]
	v_pk_mul_f32 v[34:35], v[34:35], v[32:33] op_sel_hi:[1,0]
	v_mov_b32_e32 v60, v59
	v_mov_b32_e32 v20, v63
	v_pk_mul_f32 v[20:21], v[20:21], v[32:33] op_sel_hi:[1,0]
	v_pk_mul_f32 v[0:1], v[34:35], v[220:221]
	v_pk_mul_f32 v[2:3], v[30:31], v[222:223]
	global_store_dwordx4 v[18:19], v[0:3], off offset:2048 nt
	s_nop 0
	v_pk_mul_f32 v[30:31], v[60:61], v[32:33] op_sel_hi:[1,0]
	v_pk_mul_f32 v[2:3], v[20:21], v[226:227]
	v_pk_mul_f32 v[0:1], v[30:31], v[224:225]
	global_store_dwordx4 v[18:19], v[0:3], off offset:3072 nt
	v_lshl_add_u64 v[18:19], v[18:19], 0, s[8:9]
	s_cbranch_scc1 .LBB0_1480
